# MoE-down epilogue: layer gate rows copied to LDS once per phase and read with ds_read_b128, eight row weights requested together; 14 of 16 per-unit vmcnt drains removed
# speedup vs baseline: 1.0091x; 1.0055x over previous
.LBB0_1473:
	v_readlane_b32 s14, v254, 51
	s_mul_i32 s80, s14, 0x6000
	s_lshl_b64 s[14:15], s[80:81], 2
	s_add_u32 s14, s74, s14
	s_addc_u32 s15, s75, s15
	v_lshrrev_b32_e32 v10, 1, v10
	s_add_u32 s14, s14, 0x615000
	v_and_b32_e32 v10, 24, v10
	s_addc_u32 s15, s15, 0
	v_lshlrev_b32_e32 v200, 2, v0
	v_lshrrev_b32_e32 v201, 10, v200
	v_and_b32_e32 v202, 0x3ff, v200
	v_mul_u32_u24_e32 v201, 0x1800, v201
	v_add_lshl_u32 v201, v201, v202, 2
	global_load_dwordx4 v[192:195], v201, s[14:15]
	v_add_u32_e32 v202, 0xc000, v201
	global_load_dwordx4 v[196:199], v202, s[14:15]
	v_lshlrev_b32_e32 v203, 2, v200
	v_add_u32_e32 v203, 0x21000, v203
	s_waitcnt vmcnt(0)
	ds_write_b128 v203, v[192:195]
	ds_write_b128 v203, v[196:199] offset:8192
	s_waitcnt lgkmcnt(0)
	v_lshlrev_b32_e32 v18, 6, v1
	v_lshlrev_b32_e32 v19, 1, v10
	s_movk_i32 s18, 0x3c0
	v_lshlrev_b32_e32 v20, 2, v1
	s_lshl_b32 s1, s1, 5
	v_and_or_b32 v18, v18, s18, v19
	s_lshl_b32 s17, s17, 13
	v_and_b32_e32 v20, 32, v20
	s_and_b32 s1, s1, 0x60
	s_add_i32 m0, s43, 0x18000
	v_lshl_add_u64 v[8:9], v[8:9], 0, s[78:79]
	v_bitop3_b32 v18, v18, s17, v20 bitop3:0xde
	s_lshl_b32 s17, s1, 7
	s_waitcnt vmcnt(2)
	s_barrier
	global_load_lds_dwordx4 v[8:9], off
	v_lshl_add_u64 v[6:7], v[6:7], 0, s[78:79]
	s_add_i32 m0, s43, 0x1a000
	s_add_i32 s47, s43, 0x8000
	s_add_i32 s48, s43, 0xa000
	global_load_lds_dwordx4 v[6:7], off
	v_lshl_add_u64 v[2:3], v[2:3], 0, s[78:79]
	s_mov_b32 m0, s47
	s_add_u32 s18, s34, 0x20080
	global_load_lds_dwordx4 v[2:3], off
	v_lshl_add_u64 v[2:3], v[4:5], 0, s[78:79]
	s_mov_b32 m0, s48
	s_addc_u32 s19, s35, 0
	global_load_lds_dwordx4 v[2:3], off
	s_add_i32 m0, s43, 0x1c000
	v_lshl_add_u64 v[2:3], s[18:19], 0, v[142:143]
	global_load_lds_dwordx4 v[2:3], off
	v_lshl_add_u64 v[2:3], s[18:19], 0, v[146:147]
	s_add_i32 m0, s43, 0x1e000
	v_lshl_or_b32 v19, v11, 6, v19
	global_load_lds_dwordx4 v[2:3], off
	v_lshlrev_b32_e32 v2, 13, v12
	v_and_b32_e32 v2, 0xffffc000, v2
	v_lshl_add_u32 v2, v13, 10, v2
	v_and_b32_e32 v3, 1, v12
	v_lshl_or_b32 v2, v3, 6, v2
	v_lshl_add_u32 v148, v14, 1, v2
	v_lshlrev_b32_e32 v2, 13, v15
	v_and_b32_e32 v2, 0xffffc000, v2
	v_lshl_add_u32 v2, v16, 10, v2
	v_and_b32_e32 v3, 1, v15
	v_lshlrev_b32_e32 v11, 2, v11
	s_waitcnt vmcnt(6)
	v_lshl_or_b32 v2, v3, 6, v2
	v_and_b32_e32 v11, 32, v11
	s_cmpk_lt_u32 s16, 0x100
	v_lshl_add_u32 v150, v17, 1, v2
	v_mov_b32_e32 v2, 0
	v_bitop3_b32 v182, v19, s17, v11 bitop3:0xde
	s_cselect_b64 s[16:17], -1, 0
	v_or_b32_e32 v183, s1, v10
	v_mov_b32_e32 v149, v115
	v_mov_b32_e32 v151, v115
	s_mov_b32 s1, 0
	v_add_u32_e32 v184, 0, v18
	v_mov_b32_e32 v3, v2
	v_mov_b32_e32 v4, v2
	v_mov_b32_e32 v5, v2
	v_mov_b32_e32 v10, v2
	v_mov_b32_e32 v11, v2
	v_mov_b32_e32 v12, v2
	v_mov_b32_e32 v13, v2
	v_mov_b32_e32 v14, v2
	v_mov_b32_e32 v15, v2
	v_mov_b32_e32 v16, v2
	v_mov_b32_e32 v17, v2
	v_mov_b32_e32 v18, v2
	v_mov_b32_e32 v19, v2
	v_mov_b32_e32 v20, v2
	v_mov_b32_e32 v21, v2
	v_mov_b32_e32 v22, v2
	v_mov_b32_e32 v23, v2
	v_mov_b32_e32 v24, v2
	v_mov_b32_e32 v25, v2
	v_mov_b32_e32 v26, v2
	v_mov_b32_e32 v27, v2
	v_mov_b32_e32 v28, v2
	v_mov_b32_e32 v29, v2
	v_mov_b32_e32 v30, v2
	v_mov_b32_e32 v31, v2
	v_mov_b32_e32 v32, v2
	v_mov_b32_e32 v33, v2
	v_mov_b32_e32 v34, v2
	v_mov_b32_e32 v35, v2
	v_mov_b32_e32 v36, v2
	v_mov_b32_e32 v37, v2
	v_mov_b32_e32 v38, v2
	v_mov_b32_e32 v39, v2
	v_mov_b32_e32 v40, v2
	v_mov_b32_e32 v41, v2
	v_mov_b32_e32 v42, v2
	v_mov_b32_e32 v43, v2
	v_mov_b32_e32 v44, v2
	v_mov_b32_e32 v45, v2
	v_mov_b32_e32 v46, v2
	v_mov_b32_e32 v47, v2
	v_mov_b32_e32 v48, v2
	v_mov_b32_e32 v49, v2
	v_mov_b32_e32 v50, v2
	v_mov_b32_e32 v51, v2
	v_mov_b32_e32 v52, v2
	v_mov_b32_e32 v53, v2
	v_mov_b32_e32 v54, v2
	v_mov_b32_e32 v55, v2
	v_mov_b32_e32 v56, v2
	v_mov_b32_e32 v57, v2
	v_mov_b32_e32 v58, v2
	v_mov_b32_e32 v59, v2
	v_mov_b32_e32 v60, v2
	v_mov_b32_e32 v61, v2
	v_mov_b32_e32 v62, v2
	v_mov_b32_e32 v63, v2
	v_mov_b32_e32 v64, v2
	v_mov_b32_e32 v65, v2
	v_mov_b32_e32 v66, v2
	v_mov_b32_e32 v67, v2
	v_mov_b32_e32 v68, v2
	v_mov_b32_e32 v69, v2
	v_mov_b32_e32 v70, v2
	v_mov_b32_e32 v71, v2
	v_mov_b32_e32 v72, v2
	v_mov_b32_e32 v73, v2
	v_mov_b32_e32 v74, v2
	v_mov_b32_e32 v75, v2
	v_mov_b32_e32 v76, v2
	v_mov_b32_e32 v77, v2
	v_mov_b32_e32 v78, v2
	v_mov_b32_e32 v79, v2
	v_mov_b32_e32 v80, v2
	v_mov_b32_e32 v81, v2
	v_mov_b32_e32 v82, v2
	v_mov_b32_e32 v83, v2
	v_mov_b32_e32 v84, v2
	v_mov_b32_e32 v85, v2
	v_mov_b32_e32 v86, v2
	v_mov_b32_e32 v87, v2
	v_mov_b32_e32 v88, v2
	v_mov_b32_e32 v89, v2
	v_mov_b32_e32 v90, v2
	v_mov_b32_e32 v91, v2
	v_mov_b32_e32 v92, v2
	v_mov_b32_e32 v93, v2
	v_mov_b32_e32 v94, v2
	v_mov_b32_e32 v95, v2
	v_mov_b32_e32 v96, v2
	v_mov_b32_e32 v97, v2
	v_mov_b32_e32 v98, v2
	v_mov_b32_e32 v99, v2
	v_mov_b32_e32 v100, v2
	v_mov_b32_e32 v101, v2
	v_mov_b32_e32 v102, v2
	v_mov_b32_e32 v103, v2
	v_mov_b32_e32 v104, v2
	v_mov_b32_e32 v105, v2
	v_mov_b32_e32 v106, v2
	v_mov_b32_e32 v107, v2
	v_mov_b32_e32 v108, v2
	v_mov_b32_e32 v109, v2
	v_mov_b32_e32 v110, v2
	v_mov_b32_e32 v111, v2
	v_mov_b32_e32 v112, v2
	v_mov_b32_e32 v113, v2
	v_mov_b32_e32 v116, v2
	v_mov_b32_e32 v117, v2
	v_mov_b32_e32 v118, v2
	v_mov_b32_e32 v119, v2
	v_mov_b32_e32 v120, v2
	v_mov_b32_e32 v121, v2
	v_mov_b32_e32 v122, v2
	v_mov_b32_e32 v123, v2
	v_mov_b32_e32 v124, v2
	v_mov_b32_e32 v125, v2
	v_mov_b32_e32 v126, v2
	v_mov_b32_e32 v127, v2
	v_mov_b32_e32 v128, v2
	v_mov_b32_e32 v129, v2
	v_mov_b32_e32 v130, v2
	v_mov_b32_e32 v131, v2
	v_mov_b32_e32 v6, v2
	v_mov_b32_e32 v7, v2
	v_mov_b32_e32 v8, v2
	v_mov_b32_e32 v9, v2
	s_barrier
	s_branch .LBB0_1476

.LBB0_1482:
	s_lshl_b32 s19, s0, 8
	s_and_b32 s19, s19, 0x300
	v_or_b32_e32 v187, s19, v183
	v_add_u32_e32 v152, v181, v1
	s_waitcnt vmcnt(0)
	v_and_b32_e32 v230, 0x80000001, v167
	v_cmp_eq_u32_e32 vcc, 0, v230
	s_and_saveexec_b64 s[38:39], vcc
	v_lshrrev_b32_e32 v230, 1, v167
	v_mov_b32_e32 v231, 0
	v_lshlrev_b64 v[230:231], 10, v[230:231]
	v_or_b32_e32 v230, v230, v187
	v_lshl_add_u64 v[230:231], v[230:231], 1, s[92:93]
	global_load_dwordx4 v[192:195], v[230:231], off
	global_load_dwordx4 v[196:199], v[230:231], off offset:256
	s_or_b64 exec, exec, s[38:39]
	v_and_b32_e32 v230, 0x80000001, v166
	v_cmp_eq_u32_e32 vcc, 0, v230
	s_and_saveexec_b64 s[38:39], vcc
	v_lshrrev_b32_e32 v230, 1, v166
	v_mov_b32_e32 v231, 0
	v_lshlrev_b64 v[230:231], 10, v[230:231]
	v_or_b32_e32 v230, v230, v187
	v_lshl_add_u64 v[230:231], v[230:231], 1, s[92:93]
	global_load_dwordx4 v[200:203], v[230:231], off
	global_load_dwordx4 v[204:207], v[230:231], off offset:256
	s_or_b64 exec, exec, s[38:39]
	v_and_b32_e32 v230, 0x80000001, v173
	v_cmp_eq_u32_e32 vcc, 0, v230
	s_and_saveexec_b64 s[38:39], vcc
	v_lshrrev_b32_e32 v230, 1, v173
	v_mov_b32_e32 v231, 0
	v_lshlrev_b64 v[230:231], 10, v[230:231]
	v_or_b32_e32 v230, v230, v187
	v_lshl_add_u64 v[230:231], v[230:231], 1, s[92:93]
	global_load_dwordx4 v[208:211], v[230:231], off
	global_load_dwordx4 v[212:215], v[230:231], off offset:256
	s_or_b64 exec, exec, s[38:39]
	v_and_b32_e32 v230, 0x80000001, v172
	v_cmp_eq_u32_e32 vcc, 0, v230
	s_and_saveexec_b64 s[38:39], vcc
	v_lshrrev_b32_e32 v230, 1, v172
	v_mov_b32_e32 v231, 0
	v_lshlrev_b64 v[230:231], 10, v[230:231]
	v_or_b32_e32 v230, v230, v187
	v_lshl_add_u64 v[230:231], v[230:231], 1, s[92:93]
	global_load_dwordx4 v[216:219], v[230:231], off
	global_load_dwordx4 v[220:223], v[230:231], off offset:256
	s_or_b64 exec, exec, s[38:39]
	v_and_b32_e32 v230, 0x80000001, v178
	v_cmp_eq_u32_e32 vcc, 0, v230
	s_and_saveexec_b64 s[38:39], vcc
	v_lshrrev_b32_e32 v230, 1, v178
	v_mov_b32_e32 v231, 0
	v_lshlrev_b64 v[230:231], 10, v[230:231]
	v_or_b32_e32 v230, v230, v187
	v_lshl_add_u64 v[230:231], v[230:231], 1, s[92:93]
	global_load_dwordx4 v[234:237], v[230:231], off
	global_load_dwordx4 v[238:241], v[230:231], off offset:256
	s_or_b64 exec, exec, s[38:39]
	v_and_b32_e32 v230, 0x80000001, v177
	v_cmp_eq_u32_e32 vcc, 0, v230
	s_and_saveexec_b64 s[38:39], vcc
	v_lshrrev_b32_e32 v230, 1, v177
	v_mov_b32_e32 v231, 0
	v_lshlrev_b64 v[230:231], 10, v[230:231]
	v_or_b32_e32 v230, v230, v187
	v_lshl_add_u64 v[230:231], v[230:231], 1, s[92:93]
	global_load_dwordx4 v[242:245], v[230:231], off
	global_load_dwordx4 v[246:249], v[230:231], off offset:256
	s_or_b64 exec, exec, s[38:39]
	v_cmp_lt_i32_e32 vcc, -1, v167
	v_ashrrev_i32_e32 v153, 31, v152
	v_lshlrev_b32_e32 v154, 2, v187
	v_add_u32_e32 v154, 0x21000, v154
	s_and_saveexec_b64 s[34:35], vcc
	s_cbranch_execz .LBB0_1491
	v_lshrrev_b32_e32 v114, 14, v167
	v_lshl_add_u32 v160, v114, 12, v154
	ds_read_b128 v[132:135], v160
	ds_read_b128 v[136:139], v160 offset:16
	v_readlane_b32 s36, v253, 38
	v_readlane_b32 s37, v253, 39
	s_nop 1
	v_lshl_add_u64 v[156:157], v[152:153], 2, s[36:37]
	global_load_dword v158, v[156:157], off
	global_load_dword v189, v[156:157], off offset:64
	global_load_dword v190, v[156:157], off offset:128
	global_load_dword v191, v[156:157], off offset:192
	global_load_dword v250, v[156:157], off offset:640
	global_load_dword v155, v[156:157], off offset:704
	global_load_dword v152, v[156:157], off offset:512
	global_load_dword v153, v[156:157], off offset:576
	v_lshrrev_b32_e32 v156, 1, v167
	v_mov_b32_e32 v157, v115
	v_and_b32_e32 v114, 1, v167
	v_lshlrev_b64 v[156:157], 10, v[156:157]
	v_cmp_eq_u32_e32 vcc, 1, v114
	v_or_b32_e32 v162, v156, v187
	v_mov_b32_e32 v163, v157
	s_waitcnt lgkmcnt(1)
	v_pk_mul_f32 v[134:135], v[8:9], v[134:135]
	v_pk_mul_f32 v[132:133], v[6:7], v[132:133]
	s_waitcnt lgkmcnt(0)
	v_pk_mul_f32 v[138:139], v[130:131], v[138:139]
	v_pk_mul_f32 v[168:169], v[128:129], v[136:137]
	s_waitcnt vmcnt(0)
	v_pk_mul_f32 v[164:165], v[158:159], v[134:135] op_sel_hi:[0,1]
	v_pk_mul_f32 v[136:137], v[158:159], v[132:133] op_sel_hi:[0,1]
	v_pk_mul_f32 v[138:139], v[158:159], v[138:139] op_sel_hi:[0,1]
	v_pk_mul_f32 v[132:133], v[158:159], v[168:169] op_sel_hi:[0,1]
	s_and_saveexec_b64 s[38:39], vcc
	s_xor_b64 s[38:39], exec, s[38:39]
	s_cbranch_execz .LBB0_1485
	v_cvt_pk_bf16_f32 v134, v136, v137
	v_cvt_pk_bf16_f32 v135, v164, v165
	v_cvt_pk_bf16_f32 v136, v132, v133
	v_cvt_pk_bf16_f32 v137, v138, v139
	v_lshl_add_u64 v[132:133], v[162:163], 1, s[4:5]
	global_store_dwordx4 v[132:133], v[134:137], off

.LBB0_1487:
	s_or_b64 exec, exec, s[38:39]
	ds_read_b128 v[132:135], v160 offset:512
	ds_read_b128 v[136:139], v160 offset:528
	v_mov_b32_e32 v159, v158
	s_movk_i32 s19, 0x80
	v_mov_b32_e32 v162, v158
	v_mov_b32_e32 v163, v158
	v_or3_b32 v156, v187, v156, s19
	s_waitcnt lgkmcnt(1)
	v_pk_mul_f32 v[134:135], v[100:101], v[134:135]
	v_pk_mul_f32 v[132:133], v[98:99], v[132:133]
	s_waitcnt lgkmcnt(0)
	v_pk_mul_f32 v[138:139], v[96:97], v[138:139]
	v_pk_mul_f32 v[164:165], v[94:95], v[136:137]
	v_pk_mul_f32 v[160:161], v[162:163], v[134:135]
	v_pk_mul_f32 v[136:137], v[158:159], v[132:133]
	v_pk_mul_f32 v[138:139], v[162:163], v[138:139]
	v_pk_mul_f32 v[132:133], v[158:159], v[164:165]
	s_and_saveexec_b64 s[38:39], vcc
	s_xor_b64 s[38:39], exec, s[38:39]
	s_cbranch_execz .LBB0_1489
	v_cvt_pk_bf16_f32 v134, v136, v137
	v_cvt_pk_bf16_f32 v135, v160, v161
	v_cvt_pk_bf16_f32 v136, v132, v133
	v_cvt_pk_bf16_f32 v137, v138, v139
	v_lshl_add_u64 v[132:133], v[156:157], 1, s[4:5]
	global_store_dwordx4 v[132:133], v[134:137], off

.LBB0_1491:
	s_or_b64 exec, exec, s[34:35]
	v_cmp_lt_i32_e32 vcc, -1, v166
	s_and_saveexec_b64 s[34:35], vcc
	s_cbranch_execz .LBB0_1500
	v_lshrrev_b32_e32 v114, 14, v166
	v_lshl_add_u32 v160, v114, 12, v154
	ds_read_b128 v[132:135], v160
	ds_read_b128 v[136:139], v160 offset:16
	v_mov_b32_e32 v158, v189
	v_lshrrev_b32_e32 v156, 1, v166
	v_mov_b32_e32 v157, v115
	v_and_b32_e32 v114, 1, v166
	v_lshlrev_b64 v[156:157], 10, v[156:157]
	v_cmp_eq_u32_e32 vcc, 1, v114
	v_or_b32_e32 v162, v156, v187
	v_mov_b32_e32 v163, v157
	s_waitcnt lgkmcnt(1)
	v_pk_mul_f32 v[134:135], v[126:127], v[134:135]
	v_pk_mul_f32 v[132:133], v[124:125], v[132:133]
	s_waitcnt lgkmcnt(0)
	v_pk_mul_f32 v[138:139], v[122:123], v[138:139]
	v_pk_mul_f32 v[168:169], v[120:121], v[136:137]
	v_pk_mul_f32 v[164:165], v[158:159], v[134:135] op_sel_hi:[0,1]
	v_pk_mul_f32 v[136:137], v[158:159], v[132:133] op_sel_hi:[0,1]
	v_pk_mul_f32 v[138:139], v[158:159], v[138:139] op_sel_hi:[0,1]
	v_pk_mul_f32 v[132:133], v[158:159], v[168:169] op_sel_hi:[0,1]
	s_and_saveexec_b64 s[38:39], vcc
	s_xor_b64 s[38:39], exec, s[38:39]
	s_cbranch_execz .LBB0_1494
	v_cvt_pk_bf16_f32 v134, v136, v137
	v_cvt_pk_bf16_f32 v135, v164, v165
	v_cvt_pk_bf16_f32 v136, v132, v133
	v_cvt_pk_bf16_f32 v137, v138, v139
	v_lshl_add_u64 v[132:133], v[162:163], 1, s[4:5]
	global_store_dwordx4 v[132:133], v[134:137], off

.LBB0_1496:
	s_or_b64 exec, exec, s[38:39]
	ds_read_b128 v[132:135], v160 offset:512
	ds_read_b128 v[136:139], v160 offset:528
	v_mov_b32_e32 v159, v158
	s_movk_i32 s19, 0x80
	v_mov_b32_e32 v162, v158
	v_mov_b32_e32 v163, v158
	v_or3_b32 v156, v187, v156, s19
	s_waitcnt lgkmcnt(1)
	v_pk_mul_f32 v[134:135], v[92:93], v[134:135]
	v_pk_mul_f32 v[132:133], v[90:91], v[132:133]
	s_waitcnt lgkmcnt(0)
	v_pk_mul_f32 v[138:139], v[88:89], v[138:139]
	v_pk_mul_f32 v[164:165], v[86:87], v[136:137]
	v_pk_mul_f32 v[160:161], v[162:163], v[134:135]
	v_pk_mul_f32 v[136:137], v[158:159], v[132:133]
	v_pk_mul_f32 v[138:139], v[162:163], v[138:139]
	v_pk_mul_f32 v[132:133], v[158:159], v[164:165]
	s_and_saveexec_b64 s[38:39], vcc
	s_xor_b64 s[38:39], exec, s[38:39]
	s_cbranch_execz .LBB0_1498
	v_cvt_pk_bf16_f32 v134, v136, v137
	v_cvt_pk_bf16_f32 v135, v160, v161
	v_cvt_pk_bf16_f32 v136, v132, v133
	v_cvt_pk_bf16_f32 v137, v138, v139
	v_lshl_add_u64 v[132:133], v[156:157], 1, s[4:5]
	global_store_dwordx4 v[132:133], v[134:137], off

.LBB0_1500:
	s_or_b64 exec, exec, s[34:35]
	v_and_b32_e32 v230, 0x80000001, v180
	v_cmp_eq_u32_e32 vcc, 0, v230
	s_and_saveexec_b64 s[38:39], vcc
	v_lshrrev_b32_e32 v230, 1, v180
	v_mov_b32_e32 v231, 0
	v_lshlrev_b64 v[230:231], 10, v[230:231]
	v_or_b32_e32 v230, v230, v187
	v_lshl_add_u64 v[230:231], v[230:231], 1, s[92:93]
	global_load_dwordx4 v[192:195], v[230:231], off
	global_load_dwordx4 v[196:199], v[230:231], off offset:256
	s_or_b64 exec, exec, s[38:39]
	v_and_b32_e32 v230, 0x80000001, v179
	v_cmp_eq_u32_e32 vcc, 0, v230
	s_and_saveexec_b64 s[38:39], vcc
	v_lshrrev_b32_e32 v230, 1, v179
	v_mov_b32_e32 v231, 0
	v_lshlrev_b64 v[230:231], 10, v[230:231]
	v_or_b32_e32 v230, v230, v187
	v_lshl_add_u64 v[230:231], v[230:231], 1, s[92:93]
	global_load_dwordx4 v[200:203], v[230:231], off
	global_load_dwordx4 v[204:207], v[230:231], off offset:256
	s_or_b64 exec, exec, s[38:39]
	v_cmp_lt_i32_e32 vcc, -1, v173
	s_and_saveexec_b64 s[34:35], vcc
	s_cbranch_execz .LBB0_1509
	v_lshrrev_b32_e32 v114, 14, v173
	v_lshl_add_u32 v160, v114, 12, v154
	ds_read_b128 v[132:135], v160
	ds_read_b128 v[136:139], v160 offset:16
	v_mov_b32_e32 v158, v190
	v_lshrrev_b32_e32 v156, 1, v173
	v_mov_b32_e32 v157, v115
	v_and_b32_e32 v114, 1, v173
	v_lshlrev_b64 v[156:157], 10, v[156:157]
	v_cmp_eq_u32_e32 vcc, 1, v114
	v_or_b32_e32 v162, v156, v187
	v_mov_b32_e32 v163, v157
	s_waitcnt lgkmcnt(1)
	v_pk_mul_f32 v[134:135], v[118:119], v[134:135]
	v_pk_mul_f32 v[132:133], v[116:117], v[132:133]
	s_waitcnt lgkmcnt(0)
	v_pk_mul_f32 v[138:139], v[112:113], v[138:139]
	v_pk_mul_f32 v[168:169], v[110:111], v[136:137]
	v_pk_mul_f32 v[164:165], v[158:159], v[134:135] op_sel_hi:[0,1]
	v_pk_mul_f32 v[136:137], v[158:159], v[132:133] op_sel_hi:[0,1]
	v_pk_mul_f32 v[138:139], v[158:159], v[138:139] op_sel_hi:[0,1]
	v_pk_mul_f32 v[132:133], v[158:159], v[168:169] op_sel_hi:[0,1]
	s_and_saveexec_b64 s[38:39], vcc
	s_xor_b64 s[38:39], exec, s[38:39]
	s_cbranch_execz .LBB0_1503
	v_cvt_pk_bf16_f32 v134, v136, v137
	v_cvt_pk_bf16_f32 v135, v164, v165
	v_cvt_pk_bf16_f32 v136, v132, v133
	v_cvt_pk_bf16_f32 v137, v138, v139
	v_lshl_add_u64 v[132:133], v[162:163], 1, s[4:5]
	global_store_dwordx4 v[132:133], v[134:137], off

.LBB0_1505:
	s_or_b64 exec, exec, s[38:39]
	ds_read_b128 v[132:135], v160 offset:512
	ds_read_b128 v[136:139], v160 offset:528
	v_mov_b32_e32 v159, v158
	s_movk_i32 s19, 0x80
	v_mov_b32_e32 v162, v158
	v_mov_b32_e32 v163, v158
	v_or3_b32 v156, v187, v156, s19
	s_waitcnt lgkmcnt(1)
	v_pk_mul_f32 v[134:135], v[84:85], v[134:135]
	v_pk_mul_f32 v[132:133], v[82:83], v[132:133]
	s_waitcnt lgkmcnt(0)
	v_pk_mul_f32 v[138:139], v[80:81], v[138:139]
	v_pk_mul_f32 v[164:165], v[78:79], v[136:137]
	v_pk_mul_f32 v[160:161], v[162:163], v[134:135]
	v_pk_mul_f32 v[136:137], v[158:159], v[132:133]
	v_pk_mul_f32 v[138:139], v[162:163], v[138:139]
	v_pk_mul_f32 v[132:133], v[158:159], v[164:165]
	s_and_saveexec_b64 s[38:39], vcc
	s_xor_b64 s[38:39], exec, s[38:39]
	s_cbranch_execz .LBB0_1507
	v_cvt_pk_bf16_f32 v134, v136, v137
	v_cvt_pk_bf16_f32 v135, v160, v161
	v_cvt_pk_bf16_f32 v136, v132, v133
	v_cvt_pk_bf16_f32 v137, v138, v139
	v_lshl_add_u64 v[132:133], v[156:157], 1, s[4:5]
	global_store_dwordx4 v[132:133], v[134:137], off

.LBB0_1509:
	s_or_b64 exec, exec, s[34:35]
	v_cmp_lt_i32_e32 vcc, -1, v172
	s_and_saveexec_b64 s[34:35], vcc
	s_cbranch_execz .LBB0_1518
	v_lshrrev_b32_e32 v114, 14, v172
	v_lshl_add_u32 v160, v114, 12, v154
	ds_read_b128 v[132:135], v160
	ds_read_b128 v[136:139], v160 offset:16
	v_mov_b32_e32 v158, v191
	v_lshrrev_b32_e32 v156, 1, v172
	v_mov_b32_e32 v157, v115
	v_and_b32_e32 v114, 1, v172
	v_lshlrev_b64 v[156:157], 10, v[156:157]
	v_cmp_eq_u32_e32 vcc, 1, v114
	v_or_b32_e32 v162, v156, v187
	v_mov_b32_e32 v163, v157
	s_waitcnt lgkmcnt(1)
	v_pk_mul_f32 v[134:135], v[108:109], v[134:135]
	v_pk_mul_f32 v[132:133], v[106:107], v[132:133]
	s_waitcnt lgkmcnt(0)
	v_pk_mul_f32 v[138:139], v[104:105], v[138:139]
	v_pk_mul_f32 v[168:169], v[102:103], v[136:137]
	v_pk_mul_f32 v[164:165], v[158:159], v[134:135] op_sel_hi:[0,1]
	v_pk_mul_f32 v[136:137], v[158:159], v[132:133] op_sel_hi:[0,1]
	v_pk_mul_f32 v[138:139], v[158:159], v[138:139] op_sel_hi:[0,1]
	v_pk_mul_f32 v[132:133], v[158:159], v[168:169] op_sel_hi:[0,1]
	s_and_saveexec_b64 s[38:39], vcc
	s_xor_b64 s[38:39], exec, s[38:39]
	s_cbranch_execz .LBB0_1512
	v_cvt_pk_bf16_f32 v134, v136, v137
	v_cvt_pk_bf16_f32 v135, v164, v165
	v_cvt_pk_bf16_f32 v136, v132, v133
	v_cvt_pk_bf16_f32 v137, v138, v139
	v_lshl_add_u64 v[132:133], v[162:163], 1, s[4:5]
	global_store_dwordx4 v[132:133], v[134:137], off

.LBB0_1514:
	s_or_b64 exec, exec, s[38:39]
	ds_read_b128 v[132:135], v160 offset:512
	ds_read_b128 v[136:139], v160 offset:528
	v_mov_b32_e32 v159, v158
	s_movk_i32 s19, 0x80
	v_mov_b32_e32 v162, v158
	v_mov_b32_e32 v163, v158
	v_or3_b32 v156, v187, v156, s19
	s_waitcnt lgkmcnt(1)
	v_pk_mul_f32 v[134:135], v[76:77], v[134:135]
	v_pk_mul_f32 v[132:133], v[74:75], v[132:133]
	s_waitcnt lgkmcnt(0)
	v_pk_mul_f32 v[138:139], v[72:73], v[138:139]
	v_pk_mul_f32 v[164:165], v[70:71], v[136:137]
	v_pk_mul_f32 v[160:161], v[162:163], v[134:135]
	v_pk_mul_f32 v[136:137], v[158:159], v[132:133]
	v_pk_mul_f32 v[138:139], v[162:163], v[138:139]
	v_pk_mul_f32 v[132:133], v[158:159], v[164:165]
	s_and_saveexec_b64 s[38:39], vcc
	s_xor_b64 s[38:39], exec, s[38:39]
	s_cbranch_execz .LBB0_1516
	v_cvt_pk_bf16_f32 v134, v136, v137
	v_cvt_pk_bf16_f32 v135, v160, v161
	v_cvt_pk_bf16_f32 v136, v132, v133
	v_cvt_pk_bf16_f32 v137, v138, v139
	v_lshl_add_u64 v[132:133], v[156:157], 1, s[4:5]
	global_store_dwordx4 v[132:133], v[134:137], off

.LBB0_1518:
	s_or_b64 exec, exec, s[34:35]
	v_cmp_lt_i32_e32 vcc, -1, v178
	s_and_saveexec_b64 s[34:35], vcc
	s_cbranch_execz .LBB0_1527
	v_lshrrev_b32_e32 v114, 14, v178
	v_lshl_add_u32 v160, v114, 12, v154
	ds_read_b128 v[132:135], v160
	ds_read_b128 v[136:139], v160 offset:16
	v_mov_b32_e32 v158, v152
	v_lshrrev_b32_e32 v156, 1, v178
	v_mov_b32_e32 v157, v115
	v_and_b32_e32 v114, 1, v178
	v_lshlrev_b64 v[156:157], 10, v[156:157]
	v_cmp_eq_u32_e32 vcc, 1, v114
	v_or_b32_e32 v162, v156, v187
	v_mov_b32_e32 v163, v157
	s_waitcnt lgkmcnt(1)
	v_pk_mul_f32 v[134:135], v[68:69], v[134:135]
	v_pk_mul_f32 v[132:133], v[66:67], v[132:133]
	s_waitcnt lgkmcnt(0)
	v_pk_mul_f32 v[138:139], v[64:65], v[138:139]
	v_pk_mul_f32 v[168:169], v[62:63], v[136:137]
	v_pk_mul_f32 v[164:165], v[158:159], v[134:135] op_sel_hi:[0,1]
	v_pk_mul_f32 v[136:137], v[158:159], v[132:133] op_sel_hi:[0,1]
	v_pk_mul_f32 v[138:139], v[158:159], v[138:139] op_sel_hi:[0,1]
	v_pk_mul_f32 v[132:133], v[158:159], v[168:169] op_sel_hi:[0,1]
	s_and_saveexec_b64 s[38:39], vcc
	s_xor_b64 s[38:39], exec, s[38:39]
	s_cbranch_execz .LBB0_1521
	v_cvt_pk_bf16_f32 v134, v136, v137
	v_cvt_pk_bf16_f32 v135, v164, v165
	v_cvt_pk_bf16_f32 v136, v132, v133
	v_cvt_pk_bf16_f32 v137, v138, v139
	v_lshl_add_u64 v[132:133], v[162:163], 1, s[4:5]
	global_store_dwordx4 v[132:133], v[134:137], off

.LBB0_1523:
	s_or_b64 exec, exec, s[38:39]
	ds_read_b128 v[132:135], v160 offset:512
	ds_read_b128 v[136:139], v160 offset:528
	v_mov_b32_e32 v159, v158
	s_movk_i32 s19, 0x80
	v_mov_b32_e32 v162, v158
	v_mov_b32_e32 v163, v158
	v_or3_b32 v156, v187, v156, s19
	s_waitcnt lgkmcnt(1)
	v_pk_mul_f32 v[134:135], v[36:37], v[134:135]
	v_pk_mul_f32 v[132:133], v[34:35], v[132:133]
	s_waitcnt lgkmcnt(0)
	v_pk_mul_f32 v[138:139], v[32:33], v[138:139]
	v_pk_mul_f32 v[164:165], v[30:31], v[136:137]
	v_pk_mul_f32 v[160:161], v[162:163], v[134:135]
	v_pk_mul_f32 v[136:137], v[158:159], v[132:133]
	v_pk_mul_f32 v[138:139], v[162:163], v[138:139]
	v_pk_mul_f32 v[132:133], v[158:159], v[164:165]
	s_and_saveexec_b64 s[38:39], vcc
	s_xor_b64 s[38:39], exec, s[38:39]
	s_cbranch_execz .LBB0_1525
	v_cvt_pk_bf16_f32 v134, v136, v137
	v_cvt_pk_bf16_f32 v135, v160, v161
	v_cvt_pk_bf16_f32 v136, v132, v133
	v_cvt_pk_bf16_f32 v137, v138, v139
	v_lshl_add_u64 v[132:133], v[156:157], 1, s[4:5]
	global_store_dwordx4 v[132:133], v[134:137], off

.LBB0_1527:
	s_or_b64 exec, exec, s[34:35]
	v_cmp_lt_i32_e32 vcc, -1, v177
	s_and_saveexec_b64 s[34:35], vcc
	s_cbranch_execz .LBB0_1536
	v_lshrrev_b32_e32 v114, 14, v177
	v_lshl_add_u32 v160, v114, 12, v154
	ds_read_b128 v[132:135], v160
	ds_read_b128 v[136:139], v160 offset:16
	v_mov_b32_e32 v158, v153
	v_lshrrev_b32_e32 v156, 1, v177
	v_mov_b32_e32 v157, v115
	v_and_b32_e32 v114, 1, v177
	v_lshlrev_b64 v[156:157], 10, v[156:157]
	v_cmp_eq_u32_e32 vcc, 1, v114
	v_or_b32_e32 v162, v156, v187
	v_mov_b32_e32 v163, v157
	s_waitcnt lgkmcnt(1)
	v_pk_mul_f32 v[134:135], v[60:61], v[134:135]
	v_pk_mul_f32 v[132:133], v[58:59], v[132:133]
	s_waitcnt lgkmcnt(0)
	v_pk_mul_f32 v[138:139], v[56:57], v[138:139]
	v_pk_mul_f32 v[168:169], v[54:55], v[136:137]
	v_pk_mul_f32 v[164:165], v[158:159], v[134:135] op_sel_hi:[0,1]
	v_pk_mul_f32 v[136:137], v[158:159], v[132:133] op_sel_hi:[0,1]
	v_pk_mul_f32 v[138:139], v[158:159], v[138:139] op_sel_hi:[0,1]
	v_pk_mul_f32 v[132:133], v[158:159], v[168:169] op_sel_hi:[0,1]
	s_and_saveexec_b64 s[38:39], vcc
	s_xor_b64 s[38:39], exec, s[38:39]
	s_cbranch_execz .LBB0_1530
	v_cvt_pk_bf16_f32 v134, v136, v137
	v_cvt_pk_bf16_f32 v135, v164, v165
	v_cvt_pk_bf16_f32 v136, v132, v133
	v_cvt_pk_bf16_f32 v137, v138, v139
	v_lshl_add_u64 v[132:133], v[162:163], 1, s[4:5]
	global_store_dwordx4 v[132:133], v[134:137], off

.LBB0_1532:
	s_or_b64 exec, exec, s[38:39]
	ds_read_b128 v[132:135], v160 offset:512
	ds_read_b128 v[136:139], v160 offset:528
	v_mov_b32_e32 v159, v158
	s_movk_i32 s19, 0x80
	v_mov_b32_e32 v162, v158
	v_mov_b32_e32 v163, v158
	v_or3_b32 v156, v187, v156, s19
	s_waitcnt lgkmcnt(1)
	v_pk_mul_f32 v[134:135], v[28:29], v[134:135]
	v_pk_mul_f32 v[132:133], v[26:27], v[132:133]
	s_waitcnt lgkmcnt(0)
	v_pk_mul_f32 v[138:139], v[24:25], v[138:139]
	v_pk_mul_f32 v[164:165], v[22:23], v[136:137]
	v_pk_mul_f32 v[160:161], v[162:163], v[134:135]
	v_pk_mul_f32 v[136:137], v[158:159], v[132:133]
	v_pk_mul_f32 v[138:139], v[162:163], v[138:139]
	v_pk_mul_f32 v[132:133], v[158:159], v[164:165]
	s_and_saveexec_b64 s[38:39], vcc
	s_xor_b64 s[38:39], exec, s[38:39]
	s_cbranch_execz .LBB0_1534
	v_cvt_pk_bf16_f32 v134, v136, v137
	v_cvt_pk_bf16_f32 v135, v160, v161
	v_cvt_pk_bf16_f32 v136, v132, v133
	v_cvt_pk_bf16_f32 v137, v138, v139
	v_lshl_add_u64 v[132:133], v[156:157], 1, s[4:5]
	global_store_dwordx4 v[132:133], v[134:137], off

.LBB0_1536:
	s_or_b64 exec, exec, s[34:35]
	v_cmp_lt_i32_e32 vcc, -1, v180
	s_and_saveexec_b64 s[34:35], vcc
	s_cbranch_execz .LBB0_1545
	v_lshrrev_b32_e32 v114, 14, v180
	v_lshl_add_u32 v160, v114, 12, v154
	ds_read_b128 v[132:135], v160
	ds_read_b128 v[136:139], v160 offset:16
	v_mov_b32_e32 v158, v250
	v_lshrrev_b32_e32 v156, 1, v180
	v_mov_b32_e32 v157, v115
	v_and_b32_e32 v114, 1, v180
	v_lshlrev_b64 v[156:157], 10, v[156:157]
	v_cmp_eq_u32_e32 vcc, 1, v114
	v_or_b32_e32 v162, v156, v187
	v_mov_b32_e32 v163, v157
	s_waitcnt lgkmcnt(1)
	v_pk_mul_f32 v[134:135], v[52:53], v[134:135]
	v_pk_mul_f32 v[132:133], v[50:51], v[132:133]
	s_waitcnt lgkmcnt(0)
	v_pk_mul_f32 v[138:139], v[48:49], v[138:139]
	v_pk_mul_f32 v[168:169], v[46:47], v[136:137]
	s_waitcnt vmcnt(0)
	v_pk_mul_f32 v[164:165], v[158:159], v[134:135] op_sel_hi:[0,1]
	v_pk_mul_f32 v[136:137], v[158:159], v[132:133] op_sel_hi:[0,1]
	v_pk_mul_f32 v[138:139], v[158:159], v[138:139] op_sel_hi:[0,1]
	v_pk_mul_f32 v[132:133], v[158:159], v[168:169] op_sel_hi:[0,1]
	s_and_saveexec_b64 s[38:39], vcc
	s_xor_b64 s[38:39], exec, s[38:39]
	s_cbranch_execz .LBB0_1539
	v_cvt_pk_bf16_f32 v134, v136, v137
	v_cvt_pk_bf16_f32 v135, v164, v165
	v_cvt_pk_bf16_f32 v136, v132, v133
	v_cvt_pk_bf16_f32 v137, v138, v139
	v_lshl_add_u64 v[132:133], v[162:163], 1, s[4:5]
	global_store_dwordx4 v[132:133], v[134:137], off

.LBB0_1541:
	s_or_b64 exec, exec, s[38:39]
	ds_read_b128 v[132:135], v160 offset:512
	ds_read_b128 v[136:139], v160 offset:528
	v_mov_b32_e32 v159, v158
	s_movk_i32 s19, 0x80
	v_mov_b32_e32 v162, v158
	v_mov_b32_e32 v163, v158
	v_or3_b32 v156, v187, v156, s19
	s_waitcnt lgkmcnt(1)
	v_pk_mul_f32 v[134:135], v[20:21], v[134:135]
	v_pk_mul_f32 v[132:133], v[18:19], v[132:133]
	s_waitcnt lgkmcnt(0)
	v_pk_mul_f32 v[138:139], v[16:17], v[138:139]
	v_pk_mul_f32 v[164:165], v[14:15], v[136:137]
	v_pk_mul_f32 v[160:161], v[162:163], v[134:135]
	v_pk_mul_f32 v[136:137], v[158:159], v[132:133]
	v_pk_mul_f32 v[138:139], v[162:163], v[138:139]
	v_pk_mul_f32 v[132:133], v[158:159], v[164:165]
	s_and_saveexec_b64 s[38:39], vcc
	s_xor_b64 s[38:39], exec, s[38:39]
	s_cbranch_execz .LBB0_1543
	v_cvt_pk_bf16_f32 v134, v136, v137
	v_cvt_pk_bf16_f32 v135, v160, v161
	v_cvt_pk_bf16_f32 v136, v132, v133
	v_cvt_pk_bf16_f32 v137, v138, v139
	v_lshl_add_u64 v[132:133], v[156:157], 1, s[4:5]
	global_store_dwordx4 v[132:133], v[134:137], off

.LBB0_1545:
	s_or_b64 exec, exec, s[34:35]
	v_cmp_lt_i32_e32 vcc, -1, v179
	s_and_saveexec_b64 s[34:35], vcc
	s_cbranch_execz .LBB0_1554
	v_lshrrev_b32_e32 v114, 14, v179
	v_lshl_add_u32 v156, v114, 12, v154
	ds_read_b128 v[132:135], v156
	ds_read_b128 v[136:139], v156 offset:16
	v_mov_b32_e32 v154, v155
	v_lshrrev_b32_e32 v152, 1, v179
	v_mov_b32_e32 v153, v115
	v_and_b32_e32 v114, 1, v179
	v_lshlrev_b64 v[152:153], 10, v[152:153]
	v_cmp_eq_u32_e32 vcc, 1, v114
	v_or_b32_e32 v158, v152, v187
	v_mov_b32_e32 v159, v153
	s_waitcnt lgkmcnt(1)
	v_pk_mul_f32 v[134:135], v[44:45], v[134:135]
	v_pk_mul_f32 v[132:133], v[42:43], v[132:133]
	s_waitcnt lgkmcnt(0)
	v_pk_mul_f32 v[138:139], v[40:41], v[138:139]
	v_pk_mul_f32 v[162:163], v[38:39], v[136:137]
	v_pk_mul_f32 v[160:161], v[154:155], v[134:135] op_sel_hi:[0,1]
	v_pk_mul_f32 v[136:137], v[154:155], v[132:133] op_sel_hi:[0,1]
	v_pk_mul_f32 v[138:139], v[154:155], v[138:139] op_sel_hi:[0,1]
	v_pk_mul_f32 v[132:133], v[154:155], v[162:163] op_sel_hi:[0,1]
	s_and_saveexec_b64 s[38:39], vcc
	s_xor_b64 s[38:39], exec, s[38:39]
	s_cbranch_execz .LBB0_1548
	v_cvt_pk_bf16_f32 v134, v136, v137
	v_cvt_pk_bf16_f32 v135, v160, v161
	v_cvt_pk_bf16_f32 v136, v132, v133
	v_cvt_pk_bf16_f32 v137, v138, v139
	v_lshl_add_u64 v[132:133], v[158:159], 1, s[4:5]
	global_store_dwordx4 v[132:133], v[134:137], off

.LBB0_1550:
	s_or_b64 exec, exec, s[38:39]
	ds_read_b128 v[132:135], v156 offset:512
	ds_read_b128 v[136:139], v156 offset:528
	v_mov_b32_e32 v155, v154
	s_movk_i32 s19, 0x80
	v_mov_b32_e32 v158, v154
	v_mov_b32_e32 v159, v154
	v_or3_b32 v152, v187, v152, s19
	s_waitcnt lgkmcnt(1)
	v_pk_mul_f32 v[134:135], v[12:13], v[134:135]
	v_pk_mul_f32 v[132:133], v[10:11], v[132:133]
	s_waitcnt lgkmcnt(0)
	v_pk_mul_f32 v[138:139], v[4:5], v[138:139]
	v_pk_mul_f32 v[160:161], v[2:3], v[136:137]
	v_pk_mul_f32 v[156:157], v[158:159], v[134:135]
	v_pk_mul_f32 v[136:137], v[154:155], v[132:133]
	v_pk_mul_f32 v[138:139], v[158:159], v[138:139]
	v_pk_mul_f32 v[132:133], v[154:155], v[160:161]
	s_and_saveexec_b64 s[38:39], vcc
	s_xor_b64 s[38:39], exec, s[38:39]
	s_cbranch_execz .LBB0_1552
	v_cvt_pk_bf16_f32 v134, v136, v137
	v_cvt_pk_bf16_f32 v135, v156, v157
	v_cvt_pk_bf16_f32 v136, v132, v133
	v_cvt_pk_bf16_f32 v137, v138, v139
	v_lshl_add_u64 v[132:133], v[152:153], 1, s[4:5]
	global_store_dwordx4 v[132:133], v[134:137], off

.LBB0_1554:
	s_or_b64 exec, exec, s[34:35]
	v_mov_b32_e32 v250, 0xbb800000
	s_add_u32 s34, s50, 0xffffff00
	s_addc_u32 s35, s51, -1
	s_andn2_b64 vcc, exec, s[30:31]
	s_cbranch_vccnz .LBB0_1570
	v_cmp_lt_i32_e32 vcc, v1, v185
	v_mov_b32_e32 v166, -1
	v_mov_b32_e32 v167, -1
	s_and_saveexec_b64 s[0:1], vcc
	s_cbranch_execz .LBB0_1557
	v_add_u32_e32 v2, v186, v1
	v_readlane_b32 s22, v253, 36
	v_ashrrev_i32_e32 v3, 31, v2
	v_readlane_b32 s23, v253, 37
	s_nop 1
	v_lshl_add_u64 v[2:3], v[2:3], 2, s[22:23]
	global_load_dword v167, v[2:3], off
